# PEER select top_ranks: survivor ranks via LDS-compacted key list (v_mbcnt positions, broadcast ds_read_b128, 4 VALU per survivor) instead of scalar mask walk + v_readlane
# speedup vs baseline: 1.0212x; 1.0212x over previous
; __device__ __forceinline__ void top_ranks(float sa, float sb, unsigned ka, unsigned kb, bool& ina, bool& inb, int& ra, int& rb) {
;     ...
;     ina = ka >= Lk; inb = kb >= Lk; ra = 0; rb = 0;
;     ...
;     SURV4(ka, ma) SURV4(kb, mb)
.LBB0_1090:
	s_bcnt1_i32_b64 s99, s[30:31]
	s_bcnt1_i32_b64 s98, s[12:13]
	s_add_i32 s98, s98, s99
	s_lshl_b32 s100, s46, 1
	s_add_i32 s100, s100, 0xfffe1800
	v_mbcnt_lo_u32_b32 v164, s30, 0
	v_mbcnt_hi_u32_b32 v164, s31, v164
	v_mbcnt_lo_u32_b32 v165, s12, 0
	v_mbcnt_hi_u32_b32 v165, s13, v165
	v_add_u32_e32 v165, s99, v165
	v_lshl_add_u32 v164, v164, 2, s100
	v_lshl_add_u32 v165, v165, 2, s100
	v_mbcnt_lo_u32_b32 v166, -1, 0
	v_mbcnt_hi_u32_b32 v166, -1, v166
	v_and_b32_e32 v166, 3, v166
	v_add_u32_e32 v166, s98, v166
	v_lshl_add_u32 v166, v166, 2, s100
	v_mov_b32_e32 v167, 0
	ds_write_b32 v166, v167
	s_mov_b64 exec, s[30:31]
	ds_write_b32 v164, v140
	s_mov_b64 exec, s[12:13]
	ds_write_b32 v165, v131
	s_mov_b64 exec, -1
	v_mov_b32_e32 v142, 0
	v_mov_b32_e32 v143, 0
	v_mov_b32_e32 v164, s100
	s_waitcnt lgkmcnt(0)
	ds_read_b128 v[168:171], v164
	ds_read_b128 v[172:175], v164 offset:16
	ds_read_b128 v[176:179], v164 offset:32
	ds_read_b128 v[180:183], v164 offset:48
	ds_read_b128 v[184:187], v164 offset:64
	ds_read_b128 v[188:191], v164 offset:80
	ds_read_b128 v[192:195], v164 offset:96
	ds_read_b128 v[196:199], v164 offset:112
	s_waitcnt lgkmcnt(7)
	v_cmp_gt_u32_e64 s[80:81], v168, v140
	v_cmp_gt_u32_e64 s[82:83], v168, v131
	v_cmp_gt_u32_e64 s[84:85], v169, v140
	v_cmp_gt_u32_e64 s[86:87], v169, v131
	v_addc_co_u32_e64 v142, s[96:97], 0, v142, s[80:81]
	v_addc_co_u32_e64 v143, s[96:97], 0, v143, s[82:83]
	v_addc_co_u32_e64 v142, s[96:97], 0, v142, s[84:85]
	v_addc_co_u32_e64 v143, s[96:97], 0, v143, s[86:87]
	v_cmp_gt_u32_e64 s[80:81], v170, v140
	v_cmp_gt_u32_e64 s[82:83], v170, v131
	v_cmp_gt_u32_e64 s[84:85], v171, v140
	v_cmp_gt_u32_e64 s[86:87], v171, v131
	v_addc_co_u32_e64 v142, s[96:97], 0, v142, s[80:81]
	v_addc_co_u32_e64 v143, s[96:97], 0, v143, s[82:83]
	v_addc_co_u32_e64 v142, s[96:97], 0, v142, s[84:85]
	v_addc_co_u32_e64 v143, s[96:97], 0, v143, s[86:87]
	s_cmp_le_u32 s98, 4
	s_cbranch_scc1 .Lsurv0_done
	s_waitcnt lgkmcnt(6)
	v_cmp_gt_u32_e64 s[80:81], v172, v140
	v_cmp_gt_u32_e64 s[82:83], v172, v131
	v_cmp_gt_u32_e64 s[84:85], v173, v140
	v_cmp_gt_u32_e64 s[86:87], v173, v131
	v_addc_co_u32_e64 v142, s[96:97], 0, v142, s[80:81]
	v_addc_co_u32_e64 v143, s[96:97], 0, v143, s[82:83]
	v_addc_co_u32_e64 v142, s[96:97], 0, v142, s[84:85]
	v_addc_co_u32_e64 v143, s[96:97], 0, v143, s[86:87]
	v_cmp_gt_u32_e64 s[80:81], v174, v140
	v_cmp_gt_u32_e64 s[82:83], v174, v131
	v_cmp_gt_u32_e64 s[84:85], v175, v140
	v_cmp_gt_u32_e64 s[86:87], v175, v131
	v_addc_co_u32_e64 v142, s[96:97], 0, v142, s[80:81]
	v_addc_co_u32_e64 v143, s[96:97], 0, v143, s[82:83]
	v_addc_co_u32_e64 v142, s[96:97], 0, v142, s[84:85]
	v_addc_co_u32_e64 v143, s[96:97], 0, v143, s[86:87]
	s_cmp_le_u32 s98, 8
	s_cbranch_scc1 .Lsurv0_done
	s_waitcnt lgkmcnt(5)
	v_cmp_gt_u32_e64 s[80:81], v176, v140
	v_cmp_gt_u32_e64 s[82:83], v176, v131
	v_cmp_gt_u32_e64 s[84:85], v177, v140
	v_cmp_gt_u32_e64 s[86:87], v177, v131
	v_addc_co_u32_e64 v142, s[96:97], 0, v142, s[80:81]
	v_addc_co_u32_e64 v143, s[96:97], 0, v143, s[82:83]
	v_addc_co_u32_e64 v142, s[96:97], 0, v142, s[84:85]
	v_addc_co_u32_e64 v143, s[96:97], 0, v143, s[86:87]
	v_cmp_gt_u32_e64 s[80:81], v178, v140
	v_cmp_gt_u32_e64 s[82:83], v178, v131
	v_cmp_gt_u32_e64 s[84:85], v179, v140
	v_cmp_gt_u32_e64 s[86:87], v179, v131
	v_addc_co_u32_e64 v142, s[96:97], 0, v142, s[80:81]
	v_addc_co_u32_e64 v143, s[96:97], 0, v143, s[82:83]
	v_addc_co_u32_e64 v142, s[96:97], 0, v142, s[84:85]
	v_addc_co_u32_e64 v143, s[96:97], 0, v143, s[86:87]
	s_cmp_le_u32 s98, 12
	s_cbranch_scc1 .Lsurv0_done
	s_waitcnt lgkmcnt(4)
	v_cmp_gt_u32_e64 s[80:81], v180, v140
	v_cmp_gt_u32_e64 s[82:83], v180, v131
	v_cmp_gt_u32_e64 s[84:85], v181, v140
	v_cmp_gt_u32_e64 s[86:87], v181, v131
	v_addc_co_u32_e64 v142, s[96:97], 0, v142, s[80:81]
	v_addc_co_u32_e64 v143, s[96:97], 0, v143, s[82:83]
	v_addc_co_u32_e64 v142, s[96:97], 0, v142, s[84:85]
	v_addc_co_u32_e64 v143, s[96:97], 0, v143, s[86:87]
	v_cmp_gt_u32_e64 s[80:81], v182, v140
	v_cmp_gt_u32_e64 s[82:83], v182, v131
	v_cmp_gt_u32_e64 s[84:85], v183, v140
	v_cmp_gt_u32_e64 s[86:87], v183, v131
	v_addc_co_u32_e64 v142, s[96:97], 0, v142, s[80:81]
	v_addc_co_u32_e64 v143, s[96:97], 0, v143, s[82:83]
	v_addc_co_u32_e64 v142, s[96:97], 0, v142, s[84:85]
	v_addc_co_u32_e64 v143, s[96:97], 0, v143, s[86:87]
	s_cmp_le_u32 s98, 16
	s_cbranch_scc1 .Lsurv0_done
; __device__ __forceinline__ void top_ranks(float sa, float sb, unsigned ka, unsigned kb, bool& ina, bool& inb, int& ra, int& rb) {
;     ...
;     ina = ka >= Lk; inb = kb >= Lk; ra = 0; rb = 0;
;     ...
;     SURV4(ka, ma) SURV4(kb, mb)
	s_waitcnt lgkmcnt(3)
	v_cmp_gt_u32_e64 s[80:81], v184, v140
	v_cmp_gt_u32_e64 s[82:83], v184, v131
	v_cmp_gt_u32_e64 s[84:85], v185, v140
	v_cmp_gt_u32_e64 s[86:87], v185, v131
	v_addc_co_u32_e64 v142, s[96:97], 0, v142, s[80:81]
	v_addc_co_u32_e64 v143, s[96:97], 0, v143, s[82:83]
	v_addc_co_u32_e64 v142, s[96:97], 0, v142, s[84:85]
	v_addc_co_u32_e64 v143, s[96:97], 0, v143, s[86:87]
	v_cmp_gt_u32_e64 s[80:81], v186, v140
	v_cmp_gt_u32_e64 s[82:83], v186, v131
	v_cmp_gt_u32_e64 s[84:85], v187, v140
	v_cmp_gt_u32_e64 s[86:87], v187, v131
	v_addc_co_u32_e64 v142, s[96:97], 0, v142, s[80:81]
	v_addc_co_u32_e64 v143, s[96:97], 0, v143, s[82:83]
	v_addc_co_u32_e64 v142, s[96:97], 0, v142, s[84:85]
	v_addc_co_u32_e64 v143, s[96:97], 0, v143, s[86:87]
	s_cmp_le_u32 s98, 20
	s_cbranch_scc1 .Lsurv0_done
	s_waitcnt lgkmcnt(2)
	v_cmp_gt_u32_e64 s[80:81], v188, v140
	v_cmp_gt_u32_e64 s[82:83], v188, v131
	v_cmp_gt_u32_e64 s[84:85], v189, v140
	v_cmp_gt_u32_e64 s[86:87], v189, v131
	v_addc_co_u32_e64 v142, s[96:97], 0, v142, s[80:81]
	v_addc_co_u32_e64 v143, s[96:97], 0, v143, s[82:83]
	v_addc_co_u32_e64 v142, s[96:97], 0, v142, s[84:85]
	v_addc_co_u32_e64 v143, s[96:97], 0, v143, s[86:87]
	v_cmp_gt_u32_e64 s[80:81], v190, v140
	v_cmp_gt_u32_e64 s[82:83], v190, v131
	v_cmp_gt_u32_e64 s[84:85], v191, v140
	v_cmp_gt_u32_e64 s[86:87], v191, v131
	v_addc_co_u32_e64 v142, s[96:97], 0, v142, s[80:81]
	v_addc_co_u32_e64 v143, s[96:97], 0, v143, s[82:83]
	v_addc_co_u32_e64 v142, s[96:97], 0, v142, s[84:85]
	v_addc_co_u32_e64 v143, s[96:97], 0, v143, s[86:87]
	s_cmp_le_u32 s98, 24
	s_cbranch_scc1 .Lsurv0_done
	s_waitcnt lgkmcnt(1)
	v_cmp_gt_u32_e64 s[80:81], v192, v140
	v_cmp_gt_u32_e64 s[82:83], v192, v131
	v_cmp_gt_u32_e64 s[84:85], v193, v140
	v_cmp_gt_u32_e64 s[86:87], v193, v131
	v_addc_co_u32_e64 v142, s[96:97], 0, v142, s[80:81]
	v_addc_co_u32_e64 v143, s[96:97], 0, v143, s[82:83]
	v_addc_co_u32_e64 v142, s[96:97], 0, v142, s[84:85]
	v_addc_co_u32_e64 v143, s[96:97], 0, v143, s[86:87]
	v_cmp_gt_u32_e64 s[80:81], v194, v140
	v_cmp_gt_u32_e64 s[82:83], v194, v131
	v_cmp_gt_u32_e64 s[84:85], v195, v140
	v_cmp_gt_u32_e64 s[86:87], v195, v131
	v_addc_co_u32_e64 v142, s[96:97], 0, v142, s[80:81]
	v_addc_co_u32_e64 v143, s[96:97], 0, v143, s[82:83]
	v_addc_co_u32_e64 v142, s[96:97], 0, v142, s[84:85]
	v_addc_co_u32_e64 v143, s[96:97], 0, v143, s[86:87]
	s_cmp_le_u32 s98, 28
	s_cbranch_scc1 .Lsurv0_done
	s_waitcnt lgkmcnt(0)
	v_cmp_gt_u32_e64 s[80:81], v196, v140
	v_cmp_gt_u32_e64 s[82:83], v196, v131
	v_cmp_gt_u32_e64 s[84:85], v197, v140
	v_cmp_gt_u32_e64 s[86:87], v197, v131
	v_addc_co_u32_e64 v142, s[96:97], 0, v142, s[80:81]
	v_addc_co_u32_e64 v143, s[96:97], 0, v143, s[82:83]
	v_addc_co_u32_e64 v142, s[96:97], 0, v142, s[84:85]
	v_addc_co_u32_e64 v143, s[96:97], 0, v143, s[86:87]
	v_cmp_gt_u32_e64 s[80:81], v198, v140
	v_cmp_gt_u32_e64 s[82:83], v198, v131
	v_cmp_gt_u32_e64 s[84:85], v199, v140
	v_cmp_gt_u32_e64 s[86:87], v199, v131
	v_addc_co_u32_e64 v142, s[96:97], 0, v142, s[80:81]
	v_addc_co_u32_e64 v143, s[96:97], 0, v143, s[82:83]
	v_addc_co_u32_e64 v142, s[96:97], 0, v142, s[84:85]
	v_addc_co_u32_e64 v143, s[96:97], 0, v143, s[86:87]
	s_cmp_le_u32 s98, 32
	s_cbranch_scc1 .Lsurv0_done
	s_sub_i32 s98, s98, 32
	v_add_u32_e32 v164, 0x80, v164
.Lsurv0_more:
	ds_read_b128 v[168:171], v164
	v_add_u32_e32 v164, 16, v164
	s_waitcnt lgkmcnt(0)
	v_cmp_gt_u32_e64 s[80:81], v168, v140
	v_cmp_gt_u32_e64 s[82:83], v168, v131
	v_cmp_gt_u32_e64 s[84:85], v169, v140
	v_cmp_gt_u32_e64 s[86:87], v169, v131
	v_addc_co_u32_e64 v142, s[96:97], 0, v142, s[80:81]
	v_addc_co_u32_e64 v143, s[96:97], 0, v143, s[82:83]
	v_addc_co_u32_e64 v142, s[96:97], 0, v142, s[84:85]
	v_addc_co_u32_e64 v143, s[96:97], 0, v143, s[86:87]
	v_cmp_gt_u32_e64 s[80:81], v170, v140
	v_cmp_gt_u32_e64 s[82:83], v170, v131
	v_cmp_gt_u32_e64 s[84:85], v171, v140
	v_cmp_gt_u32_e64 s[86:87], v171, v131
	v_addc_co_u32_e64 v142, s[96:97], 0, v142, s[80:81]
	v_addc_co_u32_e64 v143, s[96:97], 0, v143, s[82:83]
	v_addc_co_u32_e64 v142, s[96:97], 0, v142, s[84:85]
	v_addc_co_u32_e64 v143, s[96:97], 0, v143, s[86:87]
	s_sub_i32 s98, s98, 4
	s_cmp_gt_i32 s98, 0
	s_cbranch_scc1 .Lsurv0_more

; __device__ __forceinline__ float wave_sum_dpp(float v) {
;     v += __int_as_float(__builtin_amdgcn_update_dpp(0, __float_as_int(v), 0xB1, 0xf, 0xf, true));
;     v += __int_as_float(__builtin_amdgcn_update_dpp(0, __float_as_int(v), 0x4E, 0xf, 0xf, true));
;     v += __int_as_float(__builtin_amdgcn_update_dpp(0, __float_as_int(v), 0x124, 0xf, 0xf, true));
;     v += __int_as_float(__builtin_amdgcn_update_dpp(0, __float_as_int(v), 0x128, 0xf, 0xf, true));
;     return (__int_as_float(__builtin_amdgcn_readlane(__float_as_int(v), 0)) + __int_as_float(__builtin_amdgcn_readlane(__float_as_int(v), 16)))
;          + (__int_as_float(__builtin_amdgcn_readlane(__float_as_int(v), 32)) + __int_as_float(__builtin_amdgcn_readlane(__float_as_int(v), 48)));
; }
; __device__ __forceinline__ void top_ranks(float sa, float sb, unsigned ka, unsigned kb, bool& ina, bool& inb, int& ra, int& rb) {
;     const float tot = wave_sum_dpp(sa + sb), tsq = wave_sum_dpp(sa * sa + sb * sb);
;     const float mean = tot * (1.0f / 128.0f), sd = sqrtf(fmaxf(tsq * (1.0f / 128.0f) - mean * mean, 0.f));
;     float L = mean + 1.05f * sd;
;     unsigned long long ma, mb; unsigned Lk;
;     for (int itn = 0;; ++itn) {
;         const unsigned u = __float_as_uint(L); Lk = ((u & 0x80000000u) ? ~u : (u | 0x80000000u)) & ~127u; if (itn >= 12) Lk = 0u;
;         ma = __ballot(ka >= Lk); mb = __ballot(kb >= Lk);
;         if (__popcll(ma) + __popcll(mb) >= 16) break;
;         L -= 0.12f * sd + 1e-3f;
.LBB0_1092:
.LBB0_1094:
.LBB0_1095:
.LBB0_1096:
.LBB0_1097:
	v_lshlrev_b32_e32 v144, 16, v141
	v_and_b32_e32 v145, 0xffff0000, v141
	v_add_f32_e32 v157, v145, v144
	v_pk_mul_f32 v[160:161], v[144:145], v[144:145]
	v_not_b32_e32 v131, v144
	v_add_f32_dpp v157, v157, v157 quad_perm:[1,0,3,2] row_mask:0xf bank_mask:0xf bound_ctrl:1
	v_or_b32_e32 v136, 0x80000000, v144
	v_cmp_gt_i32_e32 vcc, 0, v144
	v_add_f32_dpp v157, v157, v157 quad_perm:[2,3,0,1] row_mask:0xf bank_mask:0xf bound_ctrl:1
	v_not_b32_e32 v140, v145
	v_cndmask_b32_e32 v131, v136, v131, vcc
	v_add_f32_dpp v157, v157, v157 row_ror:4 row_mask:0xf bank_mask:0xf bound_ctrl:1
	v_or_b32_e32 v136, 0x80000000, v145
	s_mov_b32 s34, 0
	v_add_f32_dpp v157, v157, v157 row_ror:8 row_mask:0xf bank_mask:0xf bound_ctrl:1
	v_and_or_b32 v131, v131, s49, v132
	v_readlane_b32 s10, v157, 0
	v_readlane_b32 s35, v157, 16
	v_readlane_b32 s11, v157, 32
	v_readlane_b32 s36, v157, 48
	v_add_f32_e32 v157, v160, v161
	v_mov_b32_e32 v158, s35
	v_mov_b32_e32 v159, s36
	v_add_f32_dpp v157, v157, v157 quad_perm:[1,0,3,2] row_mask:0xf bank_mask:0xf bound_ctrl:1
	v_pk_add_f32 v[158:159], s[10:11], v[158:159]
	s_nop 0
	v_add_f32_dpp v157, v157, v157 quad_perm:[2,3,0,1] row_mask:0xf bank_mask:0xf bound_ctrl:1
	v_mov_b32_e32 v161, v158
	v_mov_b32_e32 v163, v159
	v_add_f32_dpp v157, v157, v157 row_ror:4 row_mask:0xf bank_mask:0xf bound_ctrl:1
	s_nop 1
	v_add_f32_dpp v157, v157, v157 row_ror:8 row_mask:0xf bank_mask:0xf bound_ctrl:1
	s_nop 0
	v_readlane_b32 s11, v157, 16
	v_readlane_b32 s10, v157, 0
	s_nop 0
	v_mov_b32_e32 v160, s11
	v_readlane_b32 s11, v157, 48
	v_add_f32_e32 v160, s10, v160
	v_readlane_b32 s10, v157, 32
	v_mov_b32_e32 v157, s11
	s_nop 0
	v_add_f32_e32 v162, s10, v157
	v_pk_add_f32 v[158:159], v[160:161], v[162:163]
	v_cmp_gt_i32_e64 s[10:11], 0, v141
	v_pk_mul_f32 v[158:159], v[158:159], s[22:23] op_sel_hi:[1,0]
	s_nop 0
	v_fma_f32 v157, -v159, v159, v158
	v_max_f32_e32 v157, 0, v157
	v_mul_f32_e32 v158, 0x4f800000, v157
	v_cmp_gt_f32_e32 vcc, s50, v157
	v_cndmask_b32_e64 v136, v136, v140, s[10:11]
	v_and_or_b32 v136, v136, s49, v1
	v_cndmask_b32_e32 v157, v157, v158, vcc
	v_sqrt_f32_e32 v158, v157
	s_nop 0
	v_add_u32_e32 v140, -1, v158
	v_fma_f32 v141, -v140, v158, v157
	v_cmp_ge_f32_e64 s[10:11], 0, v141
	v_add_u32_e32 v141, 1, v158
	s_nop 0
	v_cndmask_b32_e64 v140, v158, v140, s[10:11]
	v_fma_f32 v158, -v141, v158, v157
	v_cmp_lt_f32_e64 s[10:11], 0, v158
	s_nop 1
	v_cndmask_b32_e64 v140, v140, v141, s[10:11]
	v_mul_f32_e32 v141, 0x37800000, v140
	v_cndmask_b32_e32 v140, v140, v141, vcc
	v_cmp_class_f32_e32 vcc, v157, v153
	s_nop 1
	v_cndmask_b32_e32 v140, v140, v157, vcc
	v_fmac_f32_e32 v159, 0x3f866666, v140
	v_fmamk_f32 v140, v140, 0x3df5c28f, v154
	v_readfirstlane_b32 s35, v159
	s_branch .LBB0_1099

; __device__ __forceinline__ void top_ranks(float sa, float sb, unsigned ka, unsigned kb, bool& ina, bool& inb, int& ra, int& rb) {
;     ...
;     ina = ka >= Lk; inb = kb >= Lk; ra = 0; rb = 0;
;     ...
;     SURV4(ka, ma) SURV4(kb, mb)
.LBB0_1101:
	s_bcnt1_i32_b64 s99, s[36:37]
	s_bcnt1_i32_b64 s98, s[10:11]
	s_add_i32 s98, s98, s99
	s_lshl_b32 s100, s46, 1
	s_add_i32 s100, s100, 0xfffe1800
	v_mbcnt_lo_u32_b32 v164, s36, 0
	v_mbcnt_hi_u32_b32 v164, s37, v164
	v_mbcnt_lo_u32_b32 v165, s10, 0
	v_mbcnt_hi_u32_b32 v165, s11, v165
	v_add_u32_e32 v165, s99, v165
	v_lshl_add_u32 v164, v164, 2, s100
	v_lshl_add_u32 v165, v165, 2, s100
	v_mbcnt_lo_u32_b32 v166, -1, 0
	v_mbcnt_hi_u32_b32 v166, -1, v166
	v_and_b32_e32 v166, 3, v166
	v_add_u32_e32 v166, s98, v166
	v_lshl_add_u32 v166, v166, 2, s100
	v_mov_b32_e32 v167, 0
	ds_write_b32 v166, v167
	s_mov_b64 exec, s[36:37]
	ds_write_b32 v164, v131
	s_mov_b64 exec, s[10:11]
	ds_write_b32 v165, v136
	s_mov_b64 exec, -1
	v_mov_b32_e32 v141, 0
	v_mov_b32_e32 v140, 0
	v_mov_b32_e32 v164, s100
	s_waitcnt lgkmcnt(0)
	ds_read_b128 v[168:171], v164
	ds_read_b128 v[172:175], v164 offset:16
	ds_read_b128 v[176:179], v164 offset:32
	ds_read_b128 v[180:183], v164 offset:48
	ds_read_b128 v[184:187], v164 offset:64
	ds_read_b128 v[188:191], v164 offset:80
	ds_read_b128 v[192:195], v164 offset:96
	ds_read_b128 v[196:199], v164 offset:112
	s_waitcnt lgkmcnt(7)
	v_cmp_gt_u32_e64 s[80:81], v168, v131
	v_cmp_gt_u32_e64 s[82:83], v168, v136
	v_cmp_gt_u32_e64 s[84:85], v169, v131
	v_cmp_gt_u32_e64 s[86:87], v169, v136
	v_addc_co_u32_e64 v141, s[96:97], 0, v141, s[80:81]
	v_addc_co_u32_e64 v140, s[96:97], 0, v140, s[82:83]
	v_addc_co_u32_e64 v141, s[96:97], 0, v141, s[84:85]
	v_addc_co_u32_e64 v140, s[96:97], 0, v140, s[86:87]
	v_cmp_gt_u32_e64 s[80:81], v170, v131
	v_cmp_gt_u32_e64 s[82:83], v170, v136
	v_cmp_gt_u32_e64 s[84:85], v171, v131
	v_cmp_gt_u32_e64 s[86:87], v171, v136
	v_addc_co_u32_e64 v141, s[96:97], 0, v141, s[80:81]
	v_addc_co_u32_e64 v140, s[96:97], 0, v140, s[82:83]
	v_addc_co_u32_e64 v141, s[96:97], 0, v141, s[84:85]
	v_addc_co_u32_e64 v140, s[96:97], 0, v140, s[86:87]
	s_cmp_le_u32 s98, 4
	s_cbranch_scc1 .Lsurv1_done
	s_waitcnt lgkmcnt(6)
	v_cmp_gt_u32_e64 s[80:81], v172, v131
	v_cmp_gt_u32_e64 s[82:83], v172, v136
	v_cmp_gt_u32_e64 s[84:85], v173, v131
	v_cmp_gt_u32_e64 s[86:87], v173, v136
	v_addc_co_u32_e64 v141, s[96:97], 0, v141, s[80:81]
	v_addc_co_u32_e64 v140, s[96:97], 0, v140, s[82:83]
	v_addc_co_u32_e64 v141, s[96:97], 0, v141, s[84:85]
	v_addc_co_u32_e64 v140, s[96:97], 0, v140, s[86:87]
	v_cmp_gt_u32_e64 s[80:81], v174, v131
	v_cmp_gt_u32_e64 s[82:83], v174, v136
	v_cmp_gt_u32_e64 s[84:85], v175, v131
	v_cmp_gt_u32_e64 s[86:87], v175, v136
	v_addc_co_u32_e64 v141, s[96:97], 0, v141, s[80:81]
	v_addc_co_u32_e64 v140, s[96:97], 0, v140, s[82:83]
	v_addc_co_u32_e64 v141, s[96:97], 0, v141, s[84:85]
	v_addc_co_u32_e64 v140, s[96:97], 0, v140, s[86:87]
	s_cmp_le_u32 s98, 8
	s_cbranch_scc1 .Lsurv1_done
	s_waitcnt lgkmcnt(5)
	v_cmp_gt_u32_e64 s[80:81], v176, v131
	v_cmp_gt_u32_e64 s[82:83], v176, v136
	v_cmp_gt_u32_e64 s[84:85], v177, v131
	v_cmp_gt_u32_e64 s[86:87], v177, v136
	v_addc_co_u32_e64 v141, s[96:97], 0, v141, s[80:81]
	v_addc_co_u32_e64 v140, s[96:97], 0, v140, s[82:83]
	v_addc_co_u32_e64 v141, s[96:97], 0, v141, s[84:85]
	v_addc_co_u32_e64 v140, s[96:97], 0, v140, s[86:87]
	v_cmp_gt_u32_e64 s[80:81], v178, v131
	v_cmp_gt_u32_e64 s[82:83], v178, v136
	v_cmp_gt_u32_e64 s[84:85], v179, v131
	v_cmp_gt_u32_e64 s[86:87], v179, v136
	v_addc_co_u32_e64 v141, s[96:97], 0, v141, s[80:81]
	v_addc_co_u32_e64 v140, s[96:97], 0, v140, s[82:83]
	v_addc_co_u32_e64 v141, s[96:97], 0, v141, s[84:85]
	v_addc_co_u32_e64 v140, s[96:97], 0, v140, s[86:87]
	s_cmp_le_u32 s98, 12
	s_cbranch_scc1 .Lsurv1_done
	s_waitcnt lgkmcnt(4)
	v_cmp_gt_u32_e64 s[80:81], v180, v131
	v_cmp_gt_u32_e64 s[82:83], v180, v136
	v_cmp_gt_u32_e64 s[84:85], v181, v131
	v_cmp_gt_u32_e64 s[86:87], v181, v136
	v_addc_co_u32_e64 v141, s[96:97], 0, v141, s[80:81]
	v_addc_co_u32_e64 v140, s[96:97], 0, v140, s[82:83]
	v_addc_co_u32_e64 v141, s[96:97], 0, v141, s[84:85]
	v_addc_co_u32_e64 v140, s[96:97], 0, v140, s[86:87]
	v_cmp_gt_u32_e64 s[80:81], v182, v131
	v_cmp_gt_u32_e64 s[82:83], v182, v136
	v_cmp_gt_u32_e64 s[84:85], v183, v131
	v_cmp_gt_u32_e64 s[86:87], v183, v136
	v_addc_co_u32_e64 v141, s[96:97], 0, v141, s[80:81]
	v_addc_co_u32_e64 v140, s[96:97], 0, v140, s[82:83]
	v_addc_co_u32_e64 v141, s[96:97], 0, v141, s[84:85]
	v_addc_co_u32_e64 v140, s[96:97], 0, v140, s[86:87]
	s_cmp_le_u32 s98, 16
	s_cbranch_scc1 .Lsurv1_done
; __device__ __forceinline__ void top_ranks(float sa, float sb, unsigned ka, unsigned kb, bool& ina, bool& inb, int& ra, int& rb) {
;     ...
;     ina = ka >= Lk; inb = kb >= Lk; ra = 0; rb = 0;
;     ...
;     SURV4(ka, ma) SURV4(kb, mb)
	s_waitcnt lgkmcnt(3)
	v_cmp_gt_u32_e64 s[80:81], v184, v131
	v_cmp_gt_u32_e64 s[82:83], v184, v136
	v_cmp_gt_u32_e64 s[84:85], v185, v131
	v_cmp_gt_u32_e64 s[86:87], v185, v136
	v_addc_co_u32_e64 v141, s[96:97], 0, v141, s[80:81]
	v_addc_co_u32_e64 v140, s[96:97], 0, v140, s[82:83]
	v_addc_co_u32_e64 v141, s[96:97], 0, v141, s[84:85]
	v_addc_co_u32_e64 v140, s[96:97], 0, v140, s[86:87]
	v_cmp_gt_u32_e64 s[80:81], v186, v131
	v_cmp_gt_u32_e64 s[82:83], v186, v136
	v_cmp_gt_u32_e64 s[84:85], v187, v131
	v_cmp_gt_u32_e64 s[86:87], v187, v136
	v_addc_co_u32_e64 v141, s[96:97], 0, v141, s[80:81]
	v_addc_co_u32_e64 v140, s[96:97], 0, v140, s[82:83]
	v_addc_co_u32_e64 v141, s[96:97], 0, v141, s[84:85]
	v_addc_co_u32_e64 v140, s[96:97], 0, v140, s[86:87]
	s_cmp_le_u32 s98, 20
	s_cbranch_scc1 .Lsurv1_done
	s_waitcnt lgkmcnt(2)
	v_cmp_gt_u32_e64 s[80:81], v188, v131
	v_cmp_gt_u32_e64 s[82:83], v188, v136
	v_cmp_gt_u32_e64 s[84:85], v189, v131
	v_cmp_gt_u32_e64 s[86:87], v189, v136
	v_addc_co_u32_e64 v141, s[96:97], 0, v141, s[80:81]
	v_addc_co_u32_e64 v140, s[96:97], 0, v140, s[82:83]
	v_addc_co_u32_e64 v141, s[96:97], 0, v141, s[84:85]
	v_addc_co_u32_e64 v140, s[96:97], 0, v140, s[86:87]
	v_cmp_gt_u32_e64 s[80:81], v190, v131
	v_cmp_gt_u32_e64 s[82:83], v190, v136
	v_cmp_gt_u32_e64 s[84:85], v191, v131
	v_cmp_gt_u32_e64 s[86:87], v191, v136
	v_addc_co_u32_e64 v141, s[96:97], 0, v141, s[80:81]
	v_addc_co_u32_e64 v140, s[96:97], 0, v140, s[82:83]
	v_addc_co_u32_e64 v141, s[96:97], 0, v141, s[84:85]
	v_addc_co_u32_e64 v140, s[96:97], 0, v140, s[86:87]
	s_cmp_le_u32 s98, 24
	s_cbranch_scc1 .Lsurv1_done
	s_waitcnt lgkmcnt(1)
	v_cmp_gt_u32_e64 s[80:81], v192, v131
	v_cmp_gt_u32_e64 s[82:83], v192, v136
	v_cmp_gt_u32_e64 s[84:85], v193, v131
	v_cmp_gt_u32_e64 s[86:87], v193, v136
	v_addc_co_u32_e64 v141, s[96:97], 0, v141, s[80:81]
	v_addc_co_u32_e64 v140, s[96:97], 0, v140, s[82:83]
	v_addc_co_u32_e64 v141, s[96:97], 0, v141, s[84:85]
	v_addc_co_u32_e64 v140, s[96:97], 0, v140, s[86:87]
	v_cmp_gt_u32_e64 s[80:81], v194, v131
	v_cmp_gt_u32_e64 s[82:83], v194, v136
	v_cmp_gt_u32_e64 s[84:85], v195, v131
	v_cmp_gt_u32_e64 s[86:87], v195, v136
	v_addc_co_u32_e64 v141, s[96:97], 0, v141, s[80:81]
	v_addc_co_u32_e64 v140, s[96:97], 0, v140, s[82:83]
	v_addc_co_u32_e64 v141, s[96:97], 0, v141, s[84:85]
	v_addc_co_u32_e64 v140, s[96:97], 0, v140, s[86:87]
	s_cmp_le_u32 s98, 28
	s_cbranch_scc1 .Lsurv1_done
	s_waitcnt lgkmcnt(0)
	v_cmp_gt_u32_e64 s[80:81], v196, v131
	v_cmp_gt_u32_e64 s[82:83], v196, v136
	v_cmp_gt_u32_e64 s[84:85], v197, v131
	v_cmp_gt_u32_e64 s[86:87], v197, v136
	v_addc_co_u32_e64 v141, s[96:97], 0, v141, s[80:81]
	v_addc_co_u32_e64 v140, s[96:97], 0, v140, s[82:83]
	v_addc_co_u32_e64 v141, s[96:97], 0, v141, s[84:85]
	v_addc_co_u32_e64 v140, s[96:97], 0, v140, s[86:87]
	v_cmp_gt_u32_e64 s[80:81], v198, v131
	v_cmp_gt_u32_e64 s[82:83], v198, v136
	v_cmp_gt_u32_e64 s[84:85], v199, v131
	v_cmp_gt_u32_e64 s[86:87], v199, v136
	v_addc_co_u32_e64 v141, s[96:97], 0, v141, s[80:81]
	v_addc_co_u32_e64 v140, s[96:97], 0, v140, s[82:83]
	v_addc_co_u32_e64 v141, s[96:97], 0, v141, s[84:85]
	v_addc_co_u32_e64 v140, s[96:97], 0, v140, s[86:87]
	s_cmp_le_u32 s98, 32
	s_cbranch_scc1 .Lsurv1_done
	s_sub_i32 s98, s98, 32
	v_add_u32_e32 v164, 0x80, v164
.Lsurv1_more:
	ds_read_b128 v[168:171], v164
	v_add_u32_e32 v164, 16, v164
	s_waitcnt lgkmcnt(0)
	v_cmp_gt_u32_e64 s[80:81], v168, v131
	v_cmp_gt_u32_e64 s[82:83], v168, v136
	v_cmp_gt_u32_e64 s[84:85], v169, v131
	v_cmp_gt_u32_e64 s[86:87], v169, v136
	v_addc_co_u32_e64 v141, s[96:97], 0, v141, s[80:81]
	v_addc_co_u32_e64 v140, s[96:97], 0, v140, s[82:83]
	v_addc_co_u32_e64 v141, s[96:97], 0, v141, s[84:85]
	v_addc_co_u32_e64 v140, s[96:97], 0, v140, s[86:87]
	v_cmp_gt_u32_e64 s[80:81], v170, v131
	v_cmp_gt_u32_e64 s[82:83], v170, v136
	v_cmp_gt_u32_e64 s[84:85], v171, v131
	v_cmp_gt_u32_e64 s[86:87], v171, v136
	v_addc_co_u32_e64 v141, s[96:97], 0, v141, s[80:81]
	v_addc_co_u32_e64 v140, s[96:97], 0, v140, s[82:83]
	v_addc_co_u32_e64 v141, s[96:97], 0, v141, s[84:85]
	v_addc_co_u32_e64 v140, s[96:97], 0, v140, s[86:87]
	s_sub_i32 s98, s98, 4
	s_cmp_gt_i32 s98, 0
	s_cbranch_scc1 .Lsurv1_more

; #define LDS_WAIT() asm volatile("s_waitcnt lgkmcnt(0)" ::: "memory")
; __device__ __forceinline__ void peer_select_phase(const Args& a, int layer, LAS unsigned char* lds, int G, int bid) {
;     ...
;         if (in1a && r1a < 16) { SV[r1a] = s1a; SI[r1a] = 2 * lane; }
;         if (in1b && r1b < 16) { SV[r1b] = s1b; SI[r1b] = 2 * lane + 1; }
;         if (in2a && r2a < 16) { SV[16 + r2a] = s2a; SI[16 + r2a] = 2 * lane; }
;         if (in2b && r2b < 16) { SV[16 + r2b] = s2b; SI[16 + r2b] = 2 * lane + 1; }
;         LDS_WAIT();
;         const float cv = SV[ci] + SV[16 + cj];
;         const unsigned ck = lane < 50 ? ord_key(cv, (unsigned)(ci * 16 + cj), 255u) : 0u;
.LBB0_1103:
.LBB0_1105:
.LBB0_1106:
	v_cmp_gt_i32_e32 vcc, 16, v142
	s_and_b64 s[34:35], s[30:31], vcc
	s_and_saveexec_b64 s[30:31], s[34:35]
	v_lshl_add_u32 v131, v142, 2, s46
	ds_write2_b32 v131, v138, v133 offset1:48
	s_or_b64 exec, exec, s[30:31]
	v_cmp_gt_i32_e32 vcc, 16, v143
	s_and_b64 s[30:31], s[12:13], vcc
	s_and_saveexec_b64 s[12:13], s[30:31]
	v_lshl_add_u32 v131, v143, 2, s46
	ds_write2_b32 v131, v139, v146 offset1:48
	s_or_b64 exec, exec, s[12:13]
	v_cmp_gt_i32_e32 vcc, 16, v141
	s_and_b64 s[30:31], s[36:37], vcc
	s_and_saveexec_b64 s[12:13], s[30:31]
	v_lshl_add_u32 v131, v141, 2, s46
	ds_write2_b32 v131, v144, v133 offset0:16 offset1:64
	s_or_b64 exec, exec, s[12:13]
	v_cmp_gt_i32_e32 vcc, 16, v140
	s_and_b64 s[12:13], s[10:11], vcc
	s_and_saveexec_b64 s[10:11], s[12:13]
	v_lshl_add_u32 v131, v140, 2, s46
	ds_write2_b32 v131, v145, v146 offset0:16 offset1:64
	s_or_b64 exec, exec, s[10:11]
	s_waitcnt lgkmcnt(0)
	ds_read_b32 v131, v147
	ds_read_b32 v136, v148 offset:64
	s_mov_b32 s10, 0
	s_waitcnt lgkmcnt(0)
	v_add_f32_e32 v131, v131, v136
	v_not_b32_e32 v136, v131
	v_or_b32_e32 v138, 0x80000000, v131
	v_cmp_gt_i32_e32 vcc, 0, v131
	s_nop 1
	v_cndmask_b32_e32 v136, v138, v136, vcc
	v_and_or_b32 v136, v136, s51, v149
	v_cndmask_b32_e64 v138, 0, v136, s[6:7]
	v_mov_b32_e32 v136, 0

; __device__ __forceinline__ void top_ranks(float sa, float sb, unsigned ka, unsigned kb, bool& ina, bool& inb, int& ra, int& rb) {
;     ...
;     ina = ka >= Lk; inb = kb >= Lk; ra = 0; rb = 0;
;     ...
;     SURV4(ka, ma) SURV4(kb, mb)
.LBB0_2151:
	s_bcnt1_i32_b64 s99, s[36:37]
	s_bcnt1_i32_b64 s98, s[12:13]
	s_add_i32 s98, s98, s99
	s_lshl_b32 s100, s50, 1
	s_add_i32 s100, s100, 0xfffe1800
	v_mbcnt_lo_u32_b32 v164, s36, 0
	v_mbcnt_hi_u32_b32 v164, s37, v164
	v_mbcnt_lo_u32_b32 v165, s12, 0
	v_mbcnt_hi_u32_b32 v165, s13, v165
	v_add_u32_e32 v165, s99, v165
	v_lshl_add_u32 v164, v164, 2, s100
	v_lshl_add_u32 v165, v165, 2, s100
	v_mbcnt_lo_u32_b32 v166, -1, 0
	v_mbcnt_hi_u32_b32 v166, -1, v166
	v_and_b32_e32 v166, 3, v166
	v_add_u32_e32 v166, s98, v166
	v_lshl_add_u32 v166, v166, 2, s100
	v_mov_b32_e32 v167, 0
	ds_write_b32 v166, v167
	s_mov_b64 exec, s[36:37]
	ds_write_b32 v164, v140
	s_mov_b64 exec, s[12:13]
	ds_write_b32 v165, v131
	s_mov_b64 exec, -1
	v_mov_b32_e32 v142, 0
	v_mov_b32_e32 v143, 0
	v_mov_b32_e32 v164, s100
	s_waitcnt lgkmcnt(0)
	ds_read_b128 v[168:171], v164
	ds_read_b128 v[172:175], v164 offset:16
	ds_read_b128 v[176:179], v164 offset:32
	ds_read_b128 v[180:183], v164 offset:48
	ds_read_b128 v[184:187], v164 offset:64
	ds_read_b128 v[188:191], v164 offset:80
	ds_read_b128 v[192:195], v164 offset:96
	ds_read_b128 v[196:199], v164 offset:112
	s_waitcnt lgkmcnt(7)
	v_cmp_gt_u32_e64 s[80:81], v168, v140
	v_cmp_gt_u32_e64 s[82:83], v168, v131
	v_cmp_gt_u32_e64 s[84:85], v169, v140
	v_cmp_gt_u32_e64 s[86:87], v169, v131
	v_addc_co_u32_e64 v142, s[96:97], 0, v142, s[80:81]
	v_addc_co_u32_e64 v143, s[96:97], 0, v143, s[82:83]
	v_addc_co_u32_e64 v142, s[96:97], 0, v142, s[84:85]
	v_addc_co_u32_e64 v143, s[96:97], 0, v143, s[86:87]
	v_cmp_gt_u32_e64 s[80:81], v170, v140
	v_cmp_gt_u32_e64 s[82:83], v170, v131
	v_cmp_gt_u32_e64 s[84:85], v171, v140
	v_cmp_gt_u32_e64 s[86:87], v171, v131
	v_addc_co_u32_e64 v142, s[96:97], 0, v142, s[80:81]
	v_addc_co_u32_e64 v143, s[96:97], 0, v143, s[82:83]
	v_addc_co_u32_e64 v142, s[96:97], 0, v142, s[84:85]
	v_addc_co_u32_e64 v143, s[96:97], 0, v143, s[86:87]
	s_cmp_le_u32 s98, 4
	s_cbranch_scc1 .Lsurv2_done
	s_waitcnt lgkmcnt(6)
	v_cmp_gt_u32_e64 s[80:81], v172, v140
	v_cmp_gt_u32_e64 s[82:83], v172, v131
	v_cmp_gt_u32_e64 s[84:85], v173, v140
	v_cmp_gt_u32_e64 s[86:87], v173, v131
	v_addc_co_u32_e64 v142, s[96:97], 0, v142, s[80:81]
	v_addc_co_u32_e64 v143, s[96:97], 0, v143, s[82:83]
	v_addc_co_u32_e64 v142, s[96:97], 0, v142, s[84:85]
	v_addc_co_u32_e64 v143, s[96:97], 0, v143, s[86:87]
	v_cmp_gt_u32_e64 s[80:81], v174, v140
	v_cmp_gt_u32_e64 s[82:83], v174, v131
	v_cmp_gt_u32_e64 s[84:85], v175, v140
	v_cmp_gt_u32_e64 s[86:87], v175, v131
	v_addc_co_u32_e64 v142, s[96:97], 0, v142, s[80:81]
	v_addc_co_u32_e64 v143, s[96:97], 0, v143, s[82:83]
	v_addc_co_u32_e64 v142, s[96:97], 0, v142, s[84:85]
	v_addc_co_u32_e64 v143, s[96:97], 0, v143, s[86:87]
	s_cmp_le_u32 s98, 8
	s_cbranch_scc1 .Lsurv2_done
	s_waitcnt lgkmcnt(5)
	v_cmp_gt_u32_e64 s[80:81], v176, v140
	v_cmp_gt_u32_e64 s[82:83], v176, v131
	v_cmp_gt_u32_e64 s[84:85], v177, v140
	v_cmp_gt_u32_e64 s[86:87], v177, v131
	v_addc_co_u32_e64 v142, s[96:97], 0, v142, s[80:81]
	v_addc_co_u32_e64 v143, s[96:97], 0, v143, s[82:83]
	v_addc_co_u32_e64 v142, s[96:97], 0, v142, s[84:85]
	v_addc_co_u32_e64 v143, s[96:97], 0, v143, s[86:87]
	v_cmp_gt_u32_e64 s[80:81], v178, v140
	v_cmp_gt_u32_e64 s[82:83], v178, v131
	v_cmp_gt_u32_e64 s[84:85], v179, v140
	v_cmp_gt_u32_e64 s[86:87], v179, v131
	v_addc_co_u32_e64 v142, s[96:97], 0, v142, s[80:81]
	v_addc_co_u32_e64 v143, s[96:97], 0, v143, s[82:83]
	v_addc_co_u32_e64 v142, s[96:97], 0, v142, s[84:85]
	v_addc_co_u32_e64 v143, s[96:97], 0, v143, s[86:87]
	s_cmp_le_u32 s98, 12
	s_cbranch_scc1 .Lsurv2_done
; __device__ __forceinline__ void top_ranks(float sa, float sb, unsigned ka, unsigned kb, bool& ina, bool& inb, int& ra, int& rb) {
;     ...
;     ina = ka >= Lk; inb = kb >= Lk; ra = 0; rb = 0;
;     ...
;     SURV4(ka, ma) SURV4(kb, mb)
	s_waitcnt lgkmcnt(4)
	v_cmp_gt_u32_e64 s[80:81], v180, v140
	v_cmp_gt_u32_e64 s[82:83], v180, v131
	v_cmp_gt_u32_e64 s[84:85], v181, v140
	v_cmp_gt_u32_e64 s[86:87], v181, v131
	v_addc_co_u32_e64 v142, s[96:97], 0, v142, s[80:81]
	v_addc_co_u32_e64 v143, s[96:97], 0, v143, s[82:83]
	v_addc_co_u32_e64 v142, s[96:97], 0, v142, s[84:85]
	v_addc_co_u32_e64 v143, s[96:97], 0, v143, s[86:87]
	v_cmp_gt_u32_e64 s[80:81], v182, v140
	v_cmp_gt_u32_e64 s[82:83], v182, v131
	v_cmp_gt_u32_e64 s[84:85], v183, v140
	v_cmp_gt_u32_e64 s[86:87], v183, v131
	v_addc_co_u32_e64 v142, s[96:97], 0, v142, s[80:81]
	v_addc_co_u32_e64 v143, s[96:97], 0, v143, s[82:83]
	v_addc_co_u32_e64 v142, s[96:97], 0, v142, s[84:85]
	v_addc_co_u32_e64 v143, s[96:97], 0, v143, s[86:87]
	s_cmp_le_u32 s98, 16
	s_cbranch_scc1 .Lsurv2_done
	s_waitcnt lgkmcnt(3)
	v_cmp_gt_u32_e64 s[80:81], v184, v140
	v_cmp_gt_u32_e64 s[82:83], v184, v131
	v_cmp_gt_u32_e64 s[84:85], v185, v140
	v_cmp_gt_u32_e64 s[86:87], v185, v131
	v_addc_co_u32_e64 v142, s[96:97], 0, v142, s[80:81]
	v_addc_co_u32_e64 v143, s[96:97], 0, v143, s[82:83]
	v_addc_co_u32_e64 v142, s[96:97], 0, v142, s[84:85]
	v_addc_co_u32_e64 v143, s[96:97], 0, v143, s[86:87]
	v_cmp_gt_u32_e64 s[80:81], v186, v140
	v_cmp_gt_u32_e64 s[82:83], v186, v131
	v_cmp_gt_u32_e64 s[84:85], v187, v140
	v_cmp_gt_u32_e64 s[86:87], v187, v131
	v_addc_co_u32_e64 v142, s[96:97], 0, v142, s[80:81]
	v_addc_co_u32_e64 v143, s[96:97], 0, v143, s[82:83]
	v_addc_co_u32_e64 v142, s[96:97], 0, v142, s[84:85]
	v_addc_co_u32_e64 v143, s[96:97], 0, v143, s[86:87]
	s_cmp_le_u32 s98, 20
	s_cbranch_scc1 .Lsurv2_done
	s_waitcnt lgkmcnt(2)
	v_cmp_gt_u32_e64 s[80:81], v188, v140
	v_cmp_gt_u32_e64 s[82:83], v188, v131
	v_cmp_gt_u32_e64 s[84:85], v189, v140
	v_cmp_gt_u32_e64 s[86:87], v189, v131
	v_addc_co_u32_e64 v142, s[96:97], 0, v142, s[80:81]
	v_addc_co_u32_e64 v143, s[96:97], 0, v143, s[82:83]
	v_addc_co_u32_e64 v142, s[96:97], 0, v142, s[84:85]
	v_addc_co_u32_e64 v143, s[96:97], 0, v143, s[86:87]
	v_cmp_gt_u32_e64 s[80:81], v190, v140
	v_cmp_gt_u32_e64 s[82:83], v190, v131
	v_cmp_gt_u32_e64 s[84:85], v191, v140
	v_cmp_gt_u32_e64 s[86:87], v191, v131
	v_addc_co_u32_e64 v142, s[96:97], 0, v142, s[80:81]
	v_addc_co_u32_e64 v143, s[96:97], 0, v143, s[82:83]
	v_addc_co_u32_e64 v142, s[96:97], 0, v142, s[84:85]
	v_addc_co_u32_e64 v143, s[96:97], 0, v143, s[86:87]
	s_cmp_le_u32 s98, 24
	s_cbranch_scc1 .Lsurv2_done
	s_waitcnt lgkmcnt(1)
	v_cmp_gt_u32_e64 s[80:81], v192, v140
	v_cmp_gt_u32_e64 s[82:83], v192, v131
	v_cmp_gt_u32_e64 s[84:85], v193, v140
	v_cmp_gt_u32_e64 s[86:87], v193, v131
	v_addc_co_u32_e64 v142, s[96:97], 0, v142, s[80:81]
	v_addc_co_u32_e64 v143, s[96:97], 0, v143, s[82:83]
	v_addc_co_u32_e64 v142, s[96:97], 0, v142, s[84:85]
	v_addc_co_u32_e64 v143, s[96:97], 0, v143, s[86:87]
	v_cmp_gt_u32_e64 s[80:81], v194, v140
	v_cmp_gt_u32_e64 s[82:83], v194, v131
	v_cmp_gt_u32_e64 s[84:85], v195, v140
	v_cmp_gt_u32_e64 s[86:87], v195, v131
	v_addc_co_u32_e64 v142, s[96:97], 0, v142, s[80:81]
	v_addc_co_u32_e64 v143, s[96:97], 0, v143, s[82:83]
	v_addc_co_u32_e64 v142, s[96:97], 0, v142, s[84:85]
	v_addc_co_u32_e64 v143, s[96:97], 0, v143, s[86:87]
	s_cmp_le_u32 s98, 28
	s_cbranch_scc1 .Lsurv2_done
	s_waitcnt lgkmcnt(0)
	v_cmp_gt_u32_e64 s[80:81], v196, v140
	v_cmp_gt_u32_e64 s[82:83], v196, v131
	v_cmp_gt_u32_e64 s[84:85], v197, v140
	v_cmp_gt_u32_e64 s[86:87], v197, v131
	v_addc_co_u32_e64 v142, s[96:97], 0, v142, s[80:81]
	v_addc_co_u32_e64 v143, s[96:97], 0, v143, s[82:83]
	v_addc_co_u32_e64 v142, s[96:97], 0, v142, s[84:85]
	v_addc_co_u32_e64 v143, s[96:97], 0, v143, s[86:87]
	v_cmp_gt_u32_e64 s[80:81], v198, v140
	v_cmp_gt_u32_e64 s[82:83], v198, v131
	v_cmp_gt_u32_e64 s[84:85], v199, v140
	v_cmp_gt_u32_e64 s[86:87], v199, v131
	v_addc_co_u32_e64 v142, s[96:97], 0, v142, s[80:81]
	v_addc_co_u32_e64 v143, s[96:97], 0, v143, s[82:83]
	v_addc_co_u32_e64 v142, s[96:97], 0, v142, s[84:85]
	v_addc_co_u32_e64 v143, s[96:97], 0, v143, s[86:87]
	s_cmp_le_u32 s98, 32
	s_cbranch_scc1 .Lsurv2_done
	s_sub_i32 s98, s98, 32
	v_add_u32_e32 v164, 0x80, v164

; __device__ __forceinline__ float wave_sum_dpp(float v) {
;     v += __int_as_float(__builtin_amdgcn_update_dpp(0, __float_as_int(v), 0xB1, 0xf, 0xf, true));
;     v += __int_as_float(__builtin_amdgcn_update_dpp(0, __float_as_int(v), 0x4E, 0xf, 0xf, true));
;     v += __int_as_float(__builtin_amdgcn_update_dpp(0, __float_as_int(v), 0x124, 0xf, 0xf, true));
;     v += __int_as_float(__builtin_amdgcn_update_dpp(0, __float_as_int(v), 0x128, 0xf, 0xf, true));
;     return (__int_as_float(__builtin_amdgcn_readlane(__float_as_int(v), 0)) + __int_as_float(__builtin_amdgcn_readlane(__float_as_int(v), 16)))
;          + (__int_as_float(__builtin_amdgcn_readlane(__float_as_int(v), 32)) + __int_as_float(__builtin_amdgcn_readlane(__float_as_int(v), 48)));
; }
; __device__ __forceinline__ void top_ranks(float sa, float sb, unsigned ka, unsigned kb, bool& ina, bool& inb, int& ra, int& rb) {
;     const float tot = wave_sum_dpp(sa + sb), tsq = wave_sum_dpp(sa * sa + sb * sb);
;     const float mean = tot * (1.0f / 128.0f), sd = sqrtf(fmaxf(tsq * (1.0f / 128.0f) - mean * mean, 0.f));
;     float L = mean + 1.05f * sd;
;     unsigned long long ma, mb; unsigned Lk;
;     for (int itn = 0;; ++itn) {
;         const unsigned u = __float_as_uint(L); Lk = ((u & 0x80000000u) ? ~u : (u | 0x80000000u)) & ~127u; if (itn >= 12) Lk = 0u;
;         ma = __ballot(ka >= Lk); mb = __ballot(kb >= Lk);
;         if (__popcll(ma) + __popcll(mb) >= 16) break;
;         L -= 0.12f * sd + 1e-3f;
.LBB0_2153:
.LBB0_2155:
.LBB0_2156:
.LBB0_2157:
.LBB0_2158:
	v_lshlrev_b32_e32 v144, 16, v141
	v_and_b32_e32 v145, 0xffff0000, v141
	v_add_f32_e32 v157, v145, v144
	v_pk_mul_f32 v[160:161], v[144:145], v[144:145]
	v_not_b32_e32 v131, v144
	v_add_f32_dpp v157, v157, v157 quad_perm:[1,0,3,2] row_mask:0xf bank_mask:0xf bound_ctrl:1
	v_or_b32_e32 v136, 0x80000000, v144
	v_cmp_gt_i32_e32 vcc, 0, v144
	v_add_f32_dpp v157, v157, v157 quad_perm:[2,3,0,1] row_mask:0xf bank_mask:0xf bound_ctrl:1
	v_not_b32_e32 v140, v145
	v_cndmask_b32_e32 v131, v136, v131, vcc
	v_add_f32_dpp v157, v157, v157 row_ror:4 row_mask:0xf bank_mask:0xf bound_ctrl:1
	v_or_b32_e32 v136, 0x80000000, v145
	s_mov_b32 s18, 0
	v_add_f32_dpp v157, v157, v157 row_ror:8 row_mask:0xf bank_mask:0xf bound_ctrl:1
	v_and_or_b32 v131, v131, s53, v132
	v_readlane_b32 s10, v157, 0
	v_readlane_b32 s34, v157, 16
	v_readlane_b32 s11, v157, 32
	v_readlane_b32 s35, v157, 48
	v_add_f32_e32 v157, v160, v161
	v_mov_b32_e32 v158, s34
	v_mov_b32_e32 v159, s35
	v_add_f32_dpp v157, v157, v157 quad_perm:[1,0,3,2] row_mask:0xf bank_mask:0xf bound_ctrl:1
	v_pk_add_f32 v[158:159], s[10:11], v[158:159]
	s_nop 0
	v_add_f32_dpp v157, v157, v157 quad_perm:[2,3,0,1] row_mask:0xf bank_mask:0xf bound_ctrl:1
	v_mov_b32_e32 v161, v158
	v_mov_b32_e32 v163, v159
	v_add_f32_dpp v157, v157, v157 row_ror:4 row_mask:0xf bank_mask:0xf bound_ctrl:1
	s_nop 1
	v_add_f32_dpp v157, v157, v157 row_ror:8 row_mask:0xf bank_mask:0xf bound_ctrl:1
	s_nop 0
	v_readlane_b32 s11, v157, 16
	v_readlane_b32 s10, v157, 0
	s_nop 0
	v_mov_b32_e32 v160, s11
	v_readlane_b32 s11, v157, 48
	v_add_f32_e32 v160, s10, v160
	v_readlane_b32 s10, v157, 32
	v_mov_b32_e32 v157, s11
	s_nop 0
	v_add_f32_e32 v162, s10, v157
	v_pk_add_f32 v[158:159], v[160:161], v[162:163]
	v_cmp_gt_i32_e64 s[10:11], 0, v141
	v_pk_mul_f32 v[158:159], v[158:159], s[24:25] op_sel_hi:[1,0]
	s_nop 0
	v_fma_f32 v157, -v159, v159, v158
	v_max_f32_e32 v157, 0, v157
	v_mul_f32_e32 v158, 0x4f800000, v157
	v_cmp_gt_f32_e32 vcc, s54, v157
	v_cndmask_b32_e64 v136, v136, v140, s[10:11]
	v_and_or_b32 v136, v136, s53, v1
	v_cndmask_b32_e32 v157, v157, v158, vcc
	v_sqrt_f32_e32 v158, v157
	s_nop 0
	v_add_u32_e32 v140, -1, v158
	v_fma_f32 v141, -v140, v158, v157
	v_cmp_ge_f32_e64 s[10:11], 0, v141
	v_add_u32_e32 v141, 1, v158
	s_nop 0
	v_cndmask_b32_e64 v140, v158, v140, s[10:11]
	v_fma_f32 v158, -v141, v158, v157
	v_cmp_lt_f32_e64 s[10:11], 0, v158
	s_nop 1
	v_cndmask_b32_e64 v140, v140, v141, s[10:11]
	v_mul_f32_e32 v141, 0x37800000, v140
	v_cndmask_b32_e32 v140, v140, v141, vcc
	v_cmp_class_f32_e32 vcc, v157, v153
	s_nop 1
	v_cndmask_b32_e32 v140, v140, v157, vcc
	v_fmac_f32_e32 v159, 0x3f866666, v140
	v_fmamk_f32 v140, v140, 0x3df5c28f, v154
	v_readfirstlane_b32 s34, v159
	s_branch .LBB0_2160

; __device__ __forceinline__ void top_ranks(float sa, float sb, unsigned ka, unsigned kb, bool& ina, bool& inb, int& ra, int& rb) {
;     ...
;     ina = ka >= Lk; inb = kb >= Lk; ra = 0; rb = 0;
;     ...
;     SURV4(ka, ma) SURV4(kb, mb)
.LBB0_2162:
	s_bcnt1_i32_b64 s99, s[38:39]
	s_bcnt1_i32_b64 s98, s[10:11]
	s_add_i32 s98, s98, s99
	s_lshl_b32 s100, s50, 1
	s_add_i32 s100, s100, 0xfffe1800
	v_mbcnt_lo_u32_b32 v164, s38, 0
	v_mbcnt_hi_u32_b32 v164, s39, v164
	v_mbcnt_lo_u32_b32 v165, s10, 0
	v_mbcnt_hi_u32_b32 v165, s11, v165
	v_add_u32_e32 v165, s99, v165
	v_lshl_add_u32 v164, v164, 2, s100
	v_lshl_add_u32 v165, v165, 2, s100
	v_mbcnt_lo_u32_b32 v166, -1, 0
	v_mbcnt_hi_u32_b32 v166, -1, v166
	v_and_b32_e32 v166, 3, v166
	v_add_u32_e32 v166, s98, v166
	v_lshl_add_u32 v166, v166, 2, s100
	v_mov_b32_e32 v167, 0
	ds_write_b32 v166, v167
	s_mov_b64 exec, s[38:39]
	ds_write_b32 v164, v131
	s_mov_b64 exec, s[10:11]
	ds_write_b32 v165, v136
	s_mov_b64 exec, -1
	v_mov_b32_e32 v141, 0
	v_mov_b32_e32 v140, 0
	v_mov_b32_e32 v164, s100
	s_waitcnt lgkmcnt(0)
	ds_read_b128 v[168:171], v164
	ds_read_b128 v[172:175], v164 offset:16
	ds_read_b128 v[176:179], v164 offset:32
	ds_read_b128 v[180:183], v164 offset:48
	ds_read_b128 v[184:187], v164 offset:64
	ds_read_b128 v[188:191], v164 offset:80
	ds_read_b128 v[192:195], v164 offset:96
	ds_read_b128 v[196:199], v164 offset:112
	s_waitcnt lgkmcnt(7)
	v_cmp_gt_u32_e64 s[80:81], v168, v131
	v_cmp_gt_u32_e64 s[82:83], v168, v136
	v_cmp_gt_u32_e64 s[84:85], v169, v131
	v_cmp_gt_u32_e64 s[86:87], v169, v136
	v_addc_co_u32_e64 v141, s[96:97], 0, v141, s[80:81]
	v_addc_co_u32_e64 v140, s[96:97], 0, v140, s[82:83]
	v_addc_co_u32_e64 v141, s[96:97], 0, v141, s[84:85]
	v_addc_co_u32_e64 v140, s[96:97], 0, v140, s[86:87]
	v_cmp_gt_u32_e64 s[80:81], v170, v131
	v_cmp_gt_u32_e64 s[82:83], v170, v136
	v_cmp_gt_u32_e64 s[84:85], v171, v131
	v_cmp_gt_u32_e64 s[86:87], v171, v136
	v_addc_co_u32_e64 v141, s[96:97], 0, v141, s[80:81]
	v_addc_co_u32_e64 v140, s[96:97], 0, v140, s[82:83]
	v_addc_co_u32_e64 v141, s[96:97], 0, v141, s[84:85]
	v_addc_co_u32_e64 v140, s[96:97], 0, v140, s[86:87]
	s_cmp_le_u32 s98, 4
	s_cbranch_scc1 .Lsurv3_done
	s_waitcnt lgkmcnt(6)
	v_cmp_gt_u32_e64 s[80:81], v172, v131
	v_cmp_gt_u32_e64 s[82:83], v172, v136
	v_cmp_gt_u32_e64 s[84:85], v173, v131
	v_cmp_gt_u32_e64 s[86:87], v173, v136
	v_addc_co_u32_e64 v141, s[96:97], 0, v141, s[80:81]
	v_addc_co_u32_e64 v140, s[96:97], 0, v140, s[82:83]
	v_addc_co_u32_e64 v141, s[96:97], 0, v141, s[84:85]
	v_addc_co_u32_e64 v140, s[96:97], 0, v140, s[86:87]
	v_cmp_gt_u32_e64 s[80:81], v174, v131
	v_cmp_gt_u32_e64 s[82:83], v174, v136
	v_cmp_gt_u32_e64 s[84:85], v175, v131
	v_cmp_gt_u32_e64 s[86:87], v175, v136
	v_addc_co_u32_e64 v141, s[96:97], 0, v141, s[80:81]
	v_addc_co_u32_e64 v140, s[96:97], 0, v140, s[82:83]
	v_addc_co_u32_e64 v141, s[96:97], 0, v141, s[84:85]
	v_addc_co_u32_e64 v140, s[96:97], 0, v140, s[86:87]
	s_cmp_le_u32 s98, 8
	s_cbranch_scc1 .Lsurv3_done
	s_waitcnt lgkmcnt(5)
	v_cmp_gt_u32_e64 s[80:81], v176, v131
	v_cmp_gt_u32_e64 s[82:83], v176, v136
	v_cmp_gt_u32_e64 s[84:85], v177, v131
	v_cmp_gt_u32_e64 s[86:87], v177, v136
	v_addc_co_u32_e64 v141, s[96:97], 0, v141, s[80:81]
	v_addc_co_u32_e64 v140, s[96:97], 0, v140, s[82:83]
	v_addc_co_u32_e64 v141, s[96:97], 0, v141, s[84:85]
	v_addc_co_u32_e64 v140, s[96:97], 0, v140, s[86:87]
	v_cmp_gt_u32_e64 s[80:81], v178, v131
	v_cmp_gt_u32_e64 s[82:83], v178, v136
	v_cmp_gt_u32_e64 s[84:85], v179, v131
	v_cmp_gt_u32_e64 s[86:87], v179, v136
	v_addc_co_u32_e64 v141, s[96:97], 0, v141, s[80:81]
	v_addc_co_u32_e64 v140, s[96:97], 0, v140, s[82:83]
	v_addc_co_u32_e64 v141, s[96:97], 0, v141, s[84:85]
	v_addc_co_u32_e64 v140, s[96:97], 0, v140, s[86:87]
	s_cmp_le_u32 s98, 12
	s_cbranch_scc1 .Lsurv3_done
; __device__ __forceinline__ void top_ranks(float sa, float sb, unsigned ka, unsigned kb, bool& ina, bool& inb, int& ra, int& rb) {
;     ...
;     ina = ka >= Lk; inb = kb >= Lk; ra = 0; rb = 0;
;     ...
;     SURV4(ka, ma) SURV4(kb, mb)
	s_waitcnt lgkmcnt(4)
	v_cmp_gt_u32_e64 s[80:81], v180, v131
	v_cmp_gt_u32_e64 s[82:83], v180, v136
	v_cmp_gt_u32_e64 s[84:85], v181, v131
	v_cmp_gt_u32_e64 s[86:87], v181, v136
	v_addc_co_u32_e64 v141, s[96:97], 0, v141, s[80:81]
	v_addc_co_u32_e64 v140, s[96:97], 0, v140, s[82:83]
	v_addc_co_u32_e64 v141, s[96:97], 0, v141, s[84:85]
	v_addc_co_u32_e64 v140, s[96:97], 0, v140, s[86:87]
	v_cmp_gt_u32_e64 s[80:81], v182, v131
	v_cmp_gt_u32_e64 s[82:83], v182, v136
	v_cmp_gt_u32_e64 s[84:85], v183, v131
	v_cmp_gt_u32_e64 s[86:87], v183, v136
	v_addc_co_u32_e64 v141, s[96:97], 0, v141, s[80:81]
	v_addc_co_u32_e64 v140, s[96:97], 0, v140, s[82:83]
	v_addc_co_u32_e64 v141, s[96:97], 0, v141, s[84:85]
	v_addc_co_u32_e64 v140, s[96:97], 0, v140, s[86:87]
	s_cmp_le_u32 s98, 16
	s_cbranch_scc1 .Lsurv3_done
	s_waitcnt lgkmcnt(3)
	v_cmp_gt_u32_e64 s[80:81], v184, v131
	v_cmp_gt_u32_e64 s[82:83], v184, v136
	v_cmp_gt_u32_e64 s[84:85], v185, v131
	v_cmp_gt_u32_e64 s[86:87], v185, v136
	v_addc_co_u32_e64 v141, s[96:97], 0, v141, s[80:81]
	v_addc_co_u32_e64 v140, s[96:97], 0, v140, s[82:83]
	v_addc_co_u32_e64 v141, s[96:97], 0, v141, s[84:85]
	v_addc_co_u32_e64 v140, s[96:97], 0, v140, s[86:87]
	v_cmp_gt_u32_e64 s[80:81], v186, v131
	v_cmp_gt_u32_e64 s[82:83], v186, v136
	v_cmp_gt_u32_e64 s[84:85], v187, v131
	v_cmp_gt_u32_e64 s[86:87], v187, v136
	v_addc_co_u32_e64 v141, s[96:97], 0, v141, s[80:81]
	v_addc_co_u32_e64 v140, s[96:97], 0, v140, s[82:83]
	v_addc_co_u32_e64 v141, s[96:97], 0, v141, s[84:85]
	v_addc_co_u32_e64 v140, s[96:97], 0, v140, s[86:87]
	s_cmp_le_u32 s98, 20
	s_cbranch_scc1 .Lsurv3_done
	s_waitcnt lgkmcnt(2)
	v_cmp_gt_u32_e64 s[80:81], v188, v131
	v_cmp_gt_u32_e64 s[82:83], v188, v136
	v_cmp_gt_u32_e64 s[84:85], v189, v131
	v_cmp_gt_u32_e64 s[86:87], v189, v136
	v_addc_co_u32_e64 v141, s[96:97], 0, v141, s[80:81]
	v_addc_co_u32_e64 v140, s[96:97], 0, v140, s[82:83]
	v_addc_co_u32_e64 v141, s[96:97], 0, v141, s[84:85]
	v_addc_co_u32_e64 v140, s[96:97], 0, v140, s[86:87]
	v_cmp_gt_u32_e64 s[80:81], v190, v131
	v_cmp_gt_u32_e64 s[82:83], v190, v136
	v_cmp_gt_u32_e64 s[84:85], v191, v131
	v_cmp_gt_u32_e64 s[86:87], v191, v136
	v_addc_co_u32_e64 v141, s[96:97], 0, v141, s[80:81]
	v_addc_co_u32_e64 v140, s[96:97], 0, v140, s[82:83]
	v_addc_co_u32_e64 v141, s[96:97], 0, v141, s[84:85]
	v_addc_co_u32_e64 v140, s[96:97], 0, v140, s[86:87]
	s_cmp_le_u32 s98, 24
	s_cbranch_scc1 .Lsurv3_done
	s_waitcnt lgkmcnt(1)
	v_cmp_gt_u32_e64 s[80:81], v192, v131
	v_cmp_gt_u32_e64 s[82:83], v192, v136
	v_cmp_gt_u32_e64 s[84:85], v193, v131
	v_cmp_gt_u32_e64 s[86:87], v193, v136
	v_addc_co_u32_e64 v141, s[96:97], 0, v141, s[80:81]
	v_addc_co_u32_e64 v140, s[96:97], 0, v140, s[82:83]
	v_addc_co_u32_e64 v141, s[96:97], 0, v141, s[84:85]
	v_addc_co_u32_e64 v140, s[96:97], 0, v140, s[86:87]
	v_cmp_gt_u32_e64 s[80:81], v194, v131
	v_cmp_gt_u32_e64 s[82:83], v194, v136
	v_cmp_gt_u32_e64 s[84:85], v195, v131
	v_cmp_gt_u32_e64 s[86:87], v195, v136
	v_addc_co_u32_e64 v141, s[96:97], 0, v141, s[80:81]
	v_addc_co_u32_e64 v140, s[96:97], 0, v140, s[82:83]
	v_addc_co_u32_e64 v141, s[96:97], 0, v141, s[84:85]
	v_addc_co_u32_e64 v140, s[96:97], 0, v140, s[86:87]
	s_cmp_le_u32 s98, 28
	s_cbranch_scc1 .Lsurv3_done
	s_waitcnt lgkmcnt(0)
	v_cmp_gt_u32_e64 s[80:81], v196, v131
	v_cmp_gt_u32_e64 s[82:83], v196, v136
	v_cmp_gt_u32_e64 s[84:85], v197, v131
	v_cmp_gt_u32_e64 s[86:87], v197, v136
	v_addc_co_u32_e64 v141, s[96:97], 0, v141, s[80:81]
	v_addc_co_u32_e64 v140, s[96:97], 0, v140, s[82:83]
	v_addc_co_u32_e64 v141, s[96:97], 0, v141, s[84:85]
	v_addc_co_u32_e64 v140, s[96:97], 0, v140, s[86:87]
	v_cmp_gt_u32_e64 s[80:81], v198, v131
	v_cmp_gt_u32_e64 s[82:83], v198, v136
	v_cmp_gt_u32_e64 s[84:85], v199, v131
	v_cmp_gt_u32_e64 s[86:87], v199, v136
	v_addc_co_u32_e64 v141, s[96:97], 0, v141, s[80:81]
	v_addc_co_u32_e64 v140, s[96:97], 0, v140, s[82:83]
	v_addc_co_u32_e64 v141, s[96:97], 0, v141, s[84:85]
	v_addc_co_u32_e64 v140, s[96:97], 0, v140, s[86:87]
	s_cmp_le_u32 s98, 32
	s_cbranch_scc1 .Lsurv3_done
	s_sub_i32 s98, s98, 32
	v_add_u32_e32 v164, 0x80, v164

; #define LDS_WAIT() asm volatile("s_waitcnt lgkmcnt(0)" ::: "memory")
; __device__ __forceinline__ void peer_select_phase(const Args& a, int layer, LAS unsigned char* lds, int G, int bid) {
;     ...
;         if (in1a && r1a < 16) { SV[r1a] = s1a; SI[r1a] = 2 * lane; }
;         if (in1b && r1b < 16) { SV[r1b] = s1b; SI[r1b] = 2 * lane + 1; }
;         if (in2a && r2a < 16) { SV[16 + r2a] = s2a; SI[16 + r2a] = 2 * lane; }
;         if (in2b && r2b < 16) { SV[16 + r2b] = s2b; SI[16 + r2b] = 2 * lane + 1; }
;         LDS_WAIT();
;         const float cv = SV[ci] + SV[16 + cj];
;         const unsigned ck = lane < 50 ? ord_key(cv, (unsigned)(ci * 16 + cj), 255u) : 0u;
.LBB0_2164:
.LBB0_2166:
.LBB0_2167:
	v_cmp_gt_i32_e32 vcc, 16, v142
	s_and_b64 s[34:35], s[36:37], vcc
	s_and_saveexec_b64 s[36:37], s[34:35]
	v_lshl_add_u32 v131, v142, 2, s50
	ds_write2_b32 v131, v138, v133 offset1:48
	s_or_b64 exec, exec, s[36:37]
	v_cmp_gt_i32_e32 vcc, 16, v143
	s_and_b64 s[34:35], s[12:13], vcc
	s_and_saveexec_b64 s[12:13], s[34:35]
	v_lshl_add_u32 v131, v143, 2, s50
	ds_write2_b32 v131, v139, v146 offset1:48
	s_or_b64 exec, exec, s[12:13]
	v_cmp_gt_i32_e32 vcc, 16, v141
	s_and_b64 s[34:35], s[38:39], vcc
	s_and_saveexec_b64 s[12:13], s[34:35]
	v_lshl_add_u32 v131, v141, 2, s50
	ds_write2_b32 v131, v144, v133 offset0:16 offset1:64
	s_or_b64 exec, exec, s[12:13]
	v_cmp_gt_i32_e32 vcc, 16, v140
	s_and_b64 s[12:13], s[10:11], vcc
	s_and_saveexec_b64 s[10:11], s[12:13]
	v_lshl_add_u32 v131, v140, 2, s50
	ds_write2_b32 v131, v145, v146 offset0:16 offset1:64
	s_or_b64 exec, exec, s[10:11]
	s_waitcnt lgkmcnt(0)
	ds_read_b32 v131, v147
	ds_read_b32 v136, v148 offset:64
	s_mov_b32 s10, 0
	s_waitcnt lgkmcnt(0)
	v_add_f32_e32 v131, v131, v136
	v_not_b32_e32 v136, v131
	v_or_b32_e32 v138, 0x80000000, v131
	v_cmp_gt_i32_e32 vcc, 0, v131
	s_nop 1
	v_cndmask_b32_e32 v136, v138, v136, vcc
	v_and_or_b32 v136, v136, s55, v149
	v_cndmask_b32_e64 v138, 0, v136, s[6:7]
	v_mov_b32_e32 v136, 0
